# stack: peel + nt + leading-half wait skip + back-edge rotation + LDS-DMA shift table + relaxed up-proj first waits
# baseline (speedup 1.0000x reference)
.LBB0_311:
	ds_read_b128 v[40:43], v100
	ds_read_b128 v[60:63], v100 offset:1024
	ds_read_b128 v[80:83], v100 offset:2048
	ds_read_b128 v[100:103], v100 offset:3072
	ds_read_b128 v[120:123], v156
	ds_read_b128 v[140:143], v156 offset:1024
	ds_read_b128 v[152:155], v156 offset:2048
	ds_read_b128 v[156:159], v156 offset:3072
	s_add_u32 s24, s0, 0xfff80080
	s_addc_u32 s25, s1, -1
	s_cmp_eq_u32 s28, 28
	s_cselect_b32 s39, s4, s25
	s_cselect_b32 s38, s5, s24
	s_cselect_b32 s25, s8, s19
	s_cselect_b32 s24, s13, s17
	v_lshl_add_u64 v[188:189], s[0:1], 0, v[168:169]
	s_add_i32 m0, s78, 0xc000
	ds_read_b128 v[172:175], v191
	ds_read_b128 v[176:179], v191 offset:1024
	ds_read_b128 v[180:183], v191 offset:2048
	ds_read_b128 v[184:187], v191 offset:3072
	ds_read_b128 v[192:195], v191 offset:4096
	ds_read_b128 v[196:199], v191 offset:5120
	ds_read_b128 v[200:203], v191 offset:6144
	ds_read_b128 v[204:207], v191 offset:7168
	global_load_lds_dwordx4 v[188:189], off
	v_lshl_add_u64 v[188:189], s[0:1], 0, v[170:171]
	s_add_i32 m0, s78, 0xe000
	s_nop 0
	global_load_lds_dwordx4 v[188:189], off
	s_waitcnt vmcnt(8)
	s_and_b64 vcc, exec, s[34:35]
	s_cbranch_vccnz .Llead_skip_0_0
	s_waitcnt lgkmcnt(0)

.Llead_skip_0_3:
	s_barrier
	s_setprio 1
	s_waitcnt lgkmcnt(0)
	v_mfma_f32_16x16x32_bf16 v[68:71], v[56:59], v[172:175], v[68:71]
	v_mfma_f32_16x16x32_bf16 v[64:67], v[80:83], v[172:175], v[64:67]
	v_mfma_f32_16x16x32_bf16 v[48:51], v[56:59], v[180:183], v[48:51]
	v_mfma_f32_16x16x32_bf16 v[44:47], v[80:83], v[180:183], v[44:47]
	v_mfma_f32_16x16x32_bf16 v[28:31], v[56:59], v[192:195], v[28:31]
	v_mfma_f32_16x16x32_bf16 v[24:27], v[80:83], v[192:195], v[24:27]
	v_mfma_f32_16x16x32_bf16 v[12:15], v[56:59], v[200:203], v[12:15]
	v_mfma_f32_16x16x32_bf16 v[8:11], v[80:83], v[200:203], v[8:11]
	v_mfma_f32_16x16x32_bf16 v[68:71], v[60:63], v[176:179], v[68:71]
	v_mfma_f32_16x16x32_bf16 v[64:67], v[100:103], v[176:179], v[64:67]
	v_mfma_f32_16x16x32_bf16 v[48:51], v[60:63], v[184:187], v[48:51]
	v_mfma_f32_16x16x32_bf16 v[44:47], v[100:103], v[184:187], v[44:47]
	v_mfma_f32_16x16x32_bf16 v[28:31], v[60:63], v[196:199], v[28:31]
	v_mfma_f32_16x16x32_bf16 v[24:27], v[100:103], v[196:199], v[24:27]
	v_mfma_f32_16x16x32_bf16 v[12:15], v[60:63], v[204:207], v[12:15]
	v_mfma_f32_16x16x32_bf16 v[8:11], v[100:103], v[204:207], v[8:11]
	s_setprio 0
	s_setprio 1
	v_mfma_f32_16x16x32_bf16 v[40:43], v[120:123], v[172:175], v[40:43]
	v_mfma_f32_16x16x32_bf16 v[56:59], v[140:143], v[176:179], v[40:43]
	v_mfma_f32_16x16x32_bf16 v[40:43], v[152:155], v[172:175], v[52:55]
	v_mfma_f32_16x16x32_bf16 v[36:39], v[120:123], v[180:183], v[36:39]
	v_mfma_f32_16x16x32_bf16 v[32:35], v[152:155], v[180:183], v[32:35]
	v_mfma_f32_16x16x32_bf16 v[20:23], v[120:123], v[192:195], v[20:23]
	v_mfma_f32_16x16x32_bf16 v[16:19], v[152:155], v[192:195], v[16:19]
	v_mfma_f32_16x16x32_bf16 v[4:7], v[120:123], v[200:203], v[4:7]
	v_mfma_f32_16x16x32_bf16 v[0:3], v[152:155], v[200:203], v[0:3]
	v_mfma_f32_16x16x32_bf16 v[52:55], v[156:159], v[176:179], v[40:43]
	v_mfma_f32_16x16x32_bf16 v[36:39], v[140:143], v[184:187], v[36:39]
	v_mfma_f32_16x16x32_bf16 v[32:35], v[156:159], v[184:187], v[32:35]
	v_mfma_f32_16x16x32_bf16 v[20:23], v[140:143], v[196:199], v[20:23]
	v_mfma_f32_16x16x32_bf16 v[16:19], v[156:159], v[196:199], v[16:19]
	v_mfma_f32_16x16x32_bf16 v[4:7], v[140:143], v[204:207], v[4:7]
	v_mfma_f32_16x16x32_bf16 v[0:3], v[156:159], v[204:207], v[0:3]
	s_setprio 0
	v_add_u32_e32 v100, s3, v190
	v_add_u32_e32 v156, s75, v190
	s_add_i32 s28, s28, 2
	s_add_u32 s17, s17, 0x10000
	s_addc_u32 s19, s19, 0
	s_add_u32 s0, s0, 0x100
	s_addc_u32 s1, s1, 0
	s_cmp_gt_u32 s28, 29
	s_barrier
	s_cbranch_scc0 .LBB0_311
	s_and_b64 vcc, exec, s[34:35]
	s_cbranch_vccz .LBB0_314
	s_barrier

.LBB0_1055:
	ds_read_b128 v[128:131], v140
	ds_read_b128 v[132:135], v140 offset:1024
	ds_read_b128 v[136:139], v140 offset:2048
	ds_read_b128 v[140:143], v140 offset:3072
	ds_read_b128 v[144:147], v156
	ds_read_b128 v[148:151], v156 offset:1024
	ds_read_b128 v[152:155], v156 offset:2048
	ds_read_b128 v[156:159], v156 offset:3072
	s_add_u32 s50, s0, 0xfff80080
	s_addc_u32 s51, s1, -1
	s_cmp_eq_u32 s80, 28
	s_cselect_b32 s53, s4, s51
	s_cselect_b32 s52, s5, s50
	s_cselect_b32 s51, s39, s55
	s_cselect_b32 s50, s41, s49
	v_lshl_add_u64 v[204:205], s[0:1], 0, v[180:181]
	s_add_i32 m0, s58, 0xc000
	ds_read_b128 v[160:163], v251
	ds_read_b128 v[164:167], v251 offset:1024
	ds_read_b128 v[168:171], v251 offset:2048
	ds_read_b128 v[184:187], v251 offset:3072
	ds_read_b128 v[188:191], v251 offset:4096
	ds_read_b128 v[192:195], v251 offset:5120
	ds_read_b128 v[196:199], v251 offset:6144
	ds_read_b128 v[200:203], v251 offset:7168
	global_load_lds_dwordx4 v[204:205], off
	v_lshl_add_u64 v[204:205], s[0:1], 0, v[182:183]
	s_add_i32 m0, s58, 0xe000
	s_nop 0
	global_load_lds_dwordx4 v[204:205], off
	s_waitcnt vmcnt(8)
	s_and_b64 vcc, exec, s[34:35]
	s_cbranch_vccnz .Llead_skip_1_0
	s_waitcnt lgkmcnt(0)

.Llead_skip_1_3:
	s_barrier
	s_setprio 1
	s_waitcnt lgkmcnt(0)
	v_mfma_f32_16x16x32_bf16 v[92:95], v[128:131], v[160:163], v[92:95]
	v_mfma_f32_16x16x32_bf16 v[88:91], v[136:139], v[160:163], v[88:91]
	v_mfma_f32_16x16x32_bf16 v[84:87], v[128:131], v[168:171], v[84:87]
	v_mfma_f32_16x16x32_bf16 v[80:83], v[136:139], v[168:171], v[80:83]
	v_mfma_f32_16x16x32_bf16 v[76:79], v[128:131], v[188:191], v[76:79]
	v_mfma_f32_16x16x32_bf16 v[72:75], v[136:139], v[188:191], v[72:75]
	v_mfma_f32_16x16x32_bf16 v[68:71], v[128:131], v[196:199], v[68:71]
	v_mfma_f32_16x16x32_bf16 v[64:67], v[136:139], v[196:199], v[64:67]
	v_mfma_f32_16x16x32_bf16 v[92:95], v[132:135], v[164:167], v[92:95]
	v_mfma_f32_16x16x32_bf16 v[88:91], v[140:143], v[164:167], v[88:91]
	v_mfma_f32_16x16x32_bf16 v[84:87], v[132:135], v[184:187], v[84:87]
	v_mfma_f32_16x16x32_bf16 v[80:83], v[140:143], v[184:187], v[80:83]
	v_mfma_f32_16x16x32_bf16 v[76:79], v[132:135], v[192:195], v[76:79]
	v_mfma_f32_16x16x32_bf16 v[72:75], v[140:143], v[192:195], v[72:75]
	v_mfma_f32_16x16x32_bf16 v[68:71], v[132:135], v[200:203], v[68:71]
	v_mfma_f32_16x16x32_bf16 v[64:67], v[140:143], v[200:203], v[64:67]
	s_setprio 0
	s_setprio 1
	v_mfma_f32_16x16x32_bf16 v[28:31], v[144:147], v[160:163], v[28:31]
	v_mfma_f32_16x16x32_bf16 v[24:27], v[152:155], v[160:163], v[24:27]
	v_mfma_f32_16x16x32_bf16 v[20:23], v[144:147], v[168:171], v[20:23]
	v_mfma_f32_16x16x32_bf16 v[16:19], v[152:155], v[168:171], v[16:19]
	v_mfma_f32_16x16x32_bf16 v[12:15], v[144:147], v[188:191], v[12:15]
	v_mfma_f32_16x16x32_bf16 v[8:11], v[152:155], v[188:191], v[8:11]
	v_mfma_f32_16x16x32_bf16 v[4:7], v[144:147], v[196:199], v[4:7]
	v_mfma_f32_16x16x32_bf16 v[0:3], v[152:155], v[196:199], v[0:3]
	v_mfma_f32_16x16x32_bf16 v[28:31], v[148:151], v[164:167], v[28:31]
	v_mfma_f32_16x16x32_bf16 v[24:27], v[156:159], v[164:167], v[24:27]
	v_mfma_f32_16x16x32_bf16 v[20:23], v[148:151], v[184:187], v[20:23]
	v_mfma_f32_16x16x32_bf16 v[16:19], v[156:159], v[184:187], v[16:19]
	v_mfma_f32_16x16x32_bf16 v[12:15], v[148:151], v[192:195], v[12:15]
	v_mfma_f32_16x16x32_bf16 v[8:11], v[156:159], v[192:195], v[8:11]
	v_mfma_f32_16x16x32_bf16 v[4:7], v[148:151], v[200:203], v[4:7]
	v_mfma_f32_16x16x32_bf16 v[0:3], v[156:159], v[200:203], v[0:3]
	s_setprio 0
	v_add_u32_e32 v140, s28, v215
	v_add_u32_e32 v156, s54, v215
	s_add_i32 s80, s80, 2
	s_add_u32 s49, s49, 0x10000
	s_addc_u32 s55, s55, 0
	s_add_u32 s0, s0, 0x100
	s_addc_u32 s1, s1, 0
	s_cmp_gt_u32 s80, 29
	s_barrier
	s_cbranch_scc0 .LBB0_1055
	v_mov_b64_e32 v[220:221], 0x1ff
	v_mov_b64_e32 v[218:219], 0x200
	s_and_b64 vcc, exec, s[34:35]
	s_cbranch_vccz .LBB0_1058
	s_barrier

.Lupw_join_1:
	s_waitcnt lgkmcnt(0)
	s_barrier
	s_setprio 1
	s_waitcnt lgkmcnt(0)
	v_mfma_f32_16x16x32_bf16 v[60:63], v[108:111], v[174:177], 0
	v_mfma_f32_16x16x32_bf16 v[56:59], v[120:123], v[174:177], 0
	v_mfma_f32_16x16x32_bf16 v[44:47], v[108:111], v[182:185], 0
	v_mfma_f32_16x16x32_bf16 v[40:43], v[120:123], v[182:185], 0
	v_mfma_f32_16x16x32_bf16 v[28:31], v[108:111], v[190:193], 0
	v_mfma_f32_16x16x32_bf16 v[24:27], v[120:123], v[190:193], 0
	v_mfma_f32_16x16x32_bf16 v[12:15], v[108:111], v[198:201], 0
	v_mfma_f32_16x16x32_bf16 v[8:11], v[120:123], v[198:201], 0
	v_mfma_f32_16x16x32_bf16 v[60:63], v[112:115], v[178:181], v[60:63]
	v_mfma_f32_16x16x32_bf16 v[56:59], v[124:127], v[178:181], v[56:59]
	v_mfma_f32_16x16x32_bf16 v[44:47], v[112:115], v[186:189], v[44:47]
	v_mfma_f32_16x16x32_bf16 v[40:43], v[124:127], v[186:189], v[40:43]
	v_mfma_f32_16x16x32_bf16 v[28:31], v[112:115], v[194:197], v[28:31]
	v_mfma_f32_16x16x32_bf16 v[24:27], v[124:127], v[194:197], v[24:27]
	v_mfma_f32_16x16x32_bf16 v[12:15], v[112:115], v[202:205], v[12:15]
	v_mfma_f32_16x16x32_bf16 v[8:11], v[124:127], v[202:205], v[8:11]
	s_setprio 0
	s_setprio 1
	v_mfma_f32_16x16x32_bf16 v[52:55], v[158:161], v[174:177], 0
	v_mfma_f32_16x16x32_bf16 v[48:51], v[166:169], v[174:177], 0
	v_mfma_f32_16x16x32_bf16 v[36:39], v[158:161], v[182:185], 0
	v_mfma_f32_16x16x32_bf16 v[32:35], v[166:169], v[182:185], 0
	v_mfma_f32_16x16x32_bf16 v[20:23], v[158:161], v[190:193], 0
	v_mfma_f32_16x16x32_bf16 v[16:19], v[166:169], v[190:193], 0
	v_mfma_f32_16x16x32_bf16 v[4:7], v[158:161], v[198:201], 0
	v_mfma_f32_16x16x32_bf16 v[0:3], v[166:169], v[198:201], 0
	v_mfma_f32_16x16x32_bf16 v[52:55], v[162:165], v[178:181], v[52:55]
	v_mfma_f32_16x16x32_bf16 v[48:51], v[170:173], v[178:181], v[48:51]
	v_mfma_f32_16x16x32_bf16 v[36:39], v[162:165], v[186:189], v[36:39]
	v_mfma_f32_16x16x32_bf16 v[32:35], v[170:173], v[186:189], v[32:35]
	v_mfma_f32_16x16x32_bf16 v[20:23], v[162:165], v[194:197], v[20:23]
	v_mfma_f32_16x16x32_bf16 v[16:19], v[170:173], v[194:197], v[16:19]
	v_mfma_f32_16x16x32_bf16 v[4:7], v[162:165], v[202:205], v[4:7]
	v_mfma_f32_16x16x32_bf16 v[0:3], v[170:173], v[202:205], v[0:3]
	s_setprio 0
	s_barrier
	v_add_u32_e32 v124, s62, v156
	v_add_u32_e32 v170, s67, v156
	ds_read_b128 v[108:111], v124
	ds_read_b128 v[112:115], v124 offset:1024
	ds_read_b128 v[120:123], v124 offset:2048
	ds_read_b128 v[124:127], v124 offset:3072
	ds_read_b128 v[158:161], v170
	ds_read_b128 v[162:165], v170 offset:1024
	ds_read_b128 v[166:169], v170 offset:2048
	ds_read_b128 v[170:173], v170 offset:3072
	s_add_u32 s0, s52, 0x4000
	s_addc_u32 s1, s53, 0
	s_mov_b32 m0, s58
	v_lshl_add_u64 v[206:207], s[0:1], 0, v[144:145]
	ds_read_b128 v[174:177], v157 offset:32768
	ds_read_b128 v[178:181], v157 offset:33792
	ds_read_b128 v[182:185], v157 offset:34816
	ds_read_b128 v[186:189], v157 offset:35840
	ds_read_b128 v[190:193], v157 offset:36864
	ds_read_b128 v[194:197], v157 offset:37888
	ds_read_b128 v[198:201], v157 offset:38912
	ds_read_b128 v[202:205], v157 offset:39936
	global_load_lds_dwordx4 v[206:207], off
	v_lshl_add_u64 v[206:207], s[0:1], 0, v[148:149]
	s_mov_b32 m0, s59
	s_nop 0
	global_load_lds_dwordx4 v[206:207], off
	s_waitcnt vmcnt(8)
	s_waitcnt lgkmcnt(0)
	s_barrier
	s_setprio 1
	s_waitcnt lgkmcnt(0)
	v_mfma_f32_16x16x32_bf16 v[140:143], v[108:111], v[174:177], v[140:143]
	v_mfma_f32_16x16x32_bf16 v[136:139], v[120:123], v[174:177], v[136:139]
	v_mfma_f32_16x16x32_bf16 v[116:119], v[108:111], v[182:185], v[116:119]
	v_mfma_f32_16x16x32_bf16 v[104:107], v[120:123], v[182:185], v[104:107]
	v_mfma_f32_16x16x32_bf16 v[92:95], v[108:111], v[190:193], v[92:95]
	v_mfma_f32_16x16x32_bf16 v[88:91], v[120:123], v[190:193], v[88:91]
	v_mfma_f32_16x16x32_bf16 v[76:79], v[108:111], v[198:201], v[76:79]
	v_mfma_f32_16x16x32_bf16 v[72:75], v[120:123], v[198:201], v[72:75]
	v_mfma_f32_16x16x32_bf16 v[140:143], v[112:115], v[178:181], v[140:143]
	v_mfma_f32_16x16x32_bf16 v[136:139], v[124:127], v[178:181], v[136:139]
	v_mfma_f32_16x16x32_bf16 v[116:119], v[112:115], v[186:189], v[116:119]
	v_mfma_f32_16x16x32_bf16 v[104:107], v[124:127], v[186:189], v[104:107]
	v_mfma_f32_16x16x32_bf16 v[92:95], v[112:115], v[194:197], v[92:95]
	v_mfma_f32_16x16x32_bf16 v[88:91], v[124:127], v[194:197], v[88:91]
	v_mfma_f32_16x16x32_bf16 v[76:79], v[112:115], v[202:205], v[76:79]
	v_mfma_f32_16x16x32_bf16 v[72:75], v[124:127], v[202:205], v[72:75]
	s_setprio 0
	s_setprio 1
	v_mfma_f32_16x16x32_bf16 v[132:135], v[158:161], v[174:177], v[132:135]
	v_mfma_f32_16x16x32_bf16 v[128:131], v[166:169], v[174:177], v[128:131]
	v_mfma_f32_16x16x32_bf16 v[100:103], v[158:161], v[182:185], v[100:103]
	v_mfma_f32_16x16x32_bf16 v[96:99], v[166:169], v[182:185], v[96:99]
	v_mfma_f32_16x16x32_bf16 v[84:87], v[158:161], v[190:193], v[84:87]
	v_mfma_f32_16x16x32_bf16 v[80:83], v[166:169], v[190:193], v[80:83]
	v_mfma_f32_16x16x32_bf16 v[68:71], v[158:161], v[198:201], v[68:71]
	v_mfma_f32_16x16x32_bf16 v[64:67], v[166:169], v[198:201], v[64:67]
	v_mfma_f32_16x16x32_bf16 v[132:135], v[162:165], v[178:181], v[132:135]
	v_mfma_f32_16x16x32_bf16 v[128:131], v[170:173], v[178:181], v[128:131]
	v_mfma_f32_16x16x32_bf16 v[100:103], v[162:165], v[186:189], v[100:103]
	v_mfma_f32_16x16x32_bf16 v[96:99], v[170:173], v[186:189], v[96:99]
	v_mfma_f32_16x16x32_bf16 v[84:87], v[162:165], v[194:197], v[84:87]
	v_mfma_f32_16x16x32_bf16 v[80:83], v[170:173], v[194:197], v[80:83]
	v_mfma_f32_16x16x32_bf16 v[68:71], v[162:165], v[202:205], v[68:71]
	v_mfma_f32_16x16x32_bf16 v[64:67], v[170:173], v[202:205], v[64:67]
	s_setprio 0
	s_barrier
	s_add_u32 s0, s50, 0x8000
	s_addc_u32 s1, s51, 0
	s_mov_b32 m0, s63
	v_lshl_add_u64 v[206:207], s[0:1], 0, v[146:147]
	ds_read_b128 v[174:177], v157 offset:49152
	ds_read_b128 v[178:181], v157 offset:50176
	ds_read_b128 v[182:185], v157 offset:51200
	ds_read_b128 v[186:189], v157 offset:52224
	ds_read_b128 v[190:193], v157 offset:53248
	ds_read_b128 v[194:197], v157 offset:54272
	ds_read_b128 v[198:201], v157 offset:55296
	ds_read_b128 v[202:205], v157 offset:56320
	global_load_lds_dwordx4 v[206:207], off
	v_lshl_add_u64 v[206:207], s[0:1], 0, v[150:151]
	s_add_u32 s0, s50, 0xc000
	s_mov_b32 m0, s64
	s_addc_u32 s1, s51, 0
	global_load_lds_dwordx4 v[206:207], off
	v_lshl_add_u64 v[206:207], s[0:1], 0, v[146:147]
	s_mov_b32 m0, s68
	s_nop 0
	global_load_lds_dwordx4 v[206:207], off
	v_lshl_add_u64 v[206:207], s[0:1], 0, v[150:151]
	s_mov_b32 m0, s69
	s_nop 0
	global_load_lds_dwordx4 v[206:207], off
	v_lshl_add_u64 v[206:207], s[48:49], 0, v[144:145]
	s_mov_b32 m0, s65
	s_nop 0
	global_load_lds_dwordx4 v[206:207], off
	v_lshl_add_u64 v[206:207], s[48:49], 0, v[148:149]
	s_mov_b32 m0, s66
	s_nop 0
	global_load_lds_dwordx4 v[206:207], off
	s_waitcnt vmcnt(8)
	s_waitcnt lgkmcnt(0)
	s_barrier
	s_setprio 1
	s_waitcnt lgkmcnt(0)
	v_mfma_f32_16x16x32_bf16 v[60:63], v[108:111], v[174:177], v[60:63]
	v_mfma_f32_16x16x32_bf16 v[56:59], v[120:123], v[174:177], v[56:59]
	v_mfma_f32_16x16x32_bf16 v[44:47], v[108:111], v[182:185], v[44:47]
	v_mfma_f32_16x16x32_bf16 v[40:43], v[120:123], v[182:185], v[40:43]
	v_mfma_f32_16x16x32_bf16 v[28:31], v[108:111], v[190:193], v[28:31]
	v_mfma_f32_16x16x32_bf16 v[24:27], v[120:123], v[190:193], v[24:27]
	v_mfma_f32_16x16x32_bf16 v[12:15], v[108:111], v[198:201], v[12:15]
	v_mfma_f32_16x16x32_bf16 v[8:11], v[120:123], v[198:201], v[8:11]
	v_mfma_f32_16x16x32_bf16 v[60:63], v[112:115], v[178:181], v[60:63]
	v_mfma_f32_16x16x32_bf16 v[56:59], v[124:127], v[178:181], v[56:59]
	v_mfma_f32_16x16x32_bf16 v[44:47], v[112:115], v[186:189], v[44:47]
	v_mfma_f32_16x16x32_bf16 v[40:43], v[124:127], v[186:189], v[40:43]
	v_mfma_f32_16x16x32_bf16 v[28:31], v[112:115], v[194:197], v[28:31]
	v_mfma_f32_16x16x32_bf16 v[24:27], v[124:127], v[194:197], v[24:27]
	v_mfma_f32_16x16x32_bf16 v[12:15], v[112:115], v[202:205], v[12:15]
	v_mfma_f32_16x16x32_bf16 v[8:11], v[124:127], v[202:205], v[8:11]
	s_setprio 0
	s_setprio 1
	v_mfma_f32_16x16x32_bf16 v[52:55], v[158:161], v[174:177], v[52:55]
	v_mfma_f32_16x16x32_bf16 v[48:51], v[166:169], v[174:177], v[48:51]
	v_mfma_f32_16x16x32_bf16 v[36:39], v[158:161], v[182:185], v[36:39]
	v_mfma_f32_16x16x32_bf16 v[32:35], v[166:169], v[182:185], v[32:35]
	v_mfma_f32_16x16x32_bf16 v[20:23], v[158:161], v[190:193], v[20:23]
	v_mfma_f32_16x16x32_bf16 v[16:19], v[166:169], v[190:193], v[16:19]
	v_mfma_f32_16x16x32_bf16 v[4:7], v[158:161], v[198:201], v[4:7]
	v_mfma_f32_16x16x32_bf16 v[0:3], v[166:169], v[198:201], v[0:3]
	v_mfma_f32_16x16x32_bf16 v[52:55], v[162:165], v[178:181], v[52:55]
	v_mfma_f32_16x16x32_bf16 v[48:51], v[170:173], v[178:181], v[48:51]
	v_mfma_f32_16x16x32_bf16 v[36:39], v[162:165], v[186:189], v[36:39]
	v_mfma_f32_16x16x32_bf16 v[32:35], v[170:173], v[186:189], v[32:35]
	v_mfma_f32_16x16x32_bf16 v[20:23], v[162:165], v[194:197], v[20:23]
	v_mfma_f32_16x16x32_bf16 v[16:19], v[170:173], v[194:197], v[16:19]
	v_mfma_f32_16x16x32_bf16 v[4:7], v[162:165], v[202:205], v[4:7]
	v_mfma_f32_16x16x32_bf16 v[0:3], v[170:173], v[202:205], v[0:3]
	s_setprio 0
	v_add_u32_e32 v124, s28, v156
	v_add_u32_e32 v170, s45, v156
	s_add_i32 s78, s78, 2
	s_add_u32 s76, s76, 0x10000
	s_addc_u32 s77, s77, 0
	s_mov_b64 s[0:1], s[46:47]
	s_cmp_gt_u32 s78, 29
	s_barrier
.LBB0_1173:
	ds_read_b128 v[108:111], v124
	ds_read_b128 v[112:115], v124 offset:1024
	ds_read_b128 v[120:123], v124 offset:2048
	ds_read_b128 v[124:127], v124 offset:3072
	ds_read_b128 v[158:161], v170
	ds_read_b128 v[162:165], v170 offset:1024
	ds_read_b128 v[166:169], v170 offset:2048
	ds_read_b128 v[170:173], v170 offset:3072
	s_add_u32 s46, s0, 0x10000
	s_addc_u32 s47, s1, 0
	s_cmp_eq_u32 s78, 28
	s_cselect_b32 s52, s5, s46
	s_cselect_b32 s53, s4, s47
	s_cselect_b32 s50, s39, s76
	s_cselect_b32 s51, s35, s77
	s_add_u32 s48, s52, 0x8000
	s_addc_u32 s49, s53, 0
	v_lshl_add_u64 v[206:207], s[0:1], 0, v[152:153]
	s_add_i32 m0, s56, 0xc000
	ds_read_b128 v[174:177], v157
	ds_read_b128 v[178:181], v157 offset:1024
	ds_read_b128 v[182:185], v157 offset:2048
	ds_read_b128 v[186:189], v157 offset:3072
	ds_read_b128 v[190:193], v157 offset:4096
	ds_read_b128 v[194:197], v157 offset:5120
	ds_read_b128 v[198:201], v157 offset:6144
	ds_read_b128 v[202:205], v157 offset:7168
	global_load_lds_dwordx4 v[206:207], off
	v_lshl_add_u64 v[206:207], s[0:1], 0, v[154:155]
	s_add_i32 m0, s56, 0xe000
	s_nop 0
	global_load_lds_dwordx4 v[206:207], off
	s_waitcnt vmcnt(8)
	s_and_b64 vcc, exec, s[24:25]
	s_cbranch_vccnz .Llead_skip_2_0
	s_waitcnt lgkmcnt(0)

.Llead_skip_2_3:
	s_barrier
	s_setprio 1
	s_waitcnt lgkmcnt(0)
	v_mfma_f32_16x16x32_bf16 v[60:63], v[108:111], v[174:177], v[60:63]
	v_mfma_f32_16x16x32_bf16 v[56:59], v[120:123], v[174:177], v[56:59]
	v_mfma_f32_16x16x32_bf16 v[44:47], v[108:111], v[182:185], v[44:47]
	v_mfma_f32_16x16x32_bf16 v[40:43], v[120:123], v[182:185], v[40:43]
	v_mfma_f32_16x16x32_bf16 v[28:31], v[108:111], v[190:193], v[28:31]
	v_mfma_f32_16x16x32_bf16 v[24:27], v[120:123], v[190:193], v[24:27]
	v_mfma_f32_16x16x32_bf16 v[12:15], v[108:111], v[198:201], v[12:15]
	v_mfma_f32_16x16x32_bf16 v[8:11], v[120:123], v[198:201], v[8:11]
	v_mfma_f32_16x16x32_bf16 v[60:63], v[112:115], v[178:181], v[60:63]
	v_mfma_f32_16x16x32_bf16 v[56:59], v[124:127], v[178:181], v[56:59]
	v_mfma_f32_16x16x32_bf16 v[44:47], v[112:115], v[186:189], v[44:47]
	v_mfma_f32_16x16x32_bf16 v[40:43], v[124:127], v[186:189], v[40:43]
	v_mfma_f32_16x16x32_bf16 v[28:31], v[112:115], v[194:197], v[28:31]
	v_mfma_f32_16x16x32_bf16 v[24:27], v[124:127], v[194:197], v[24:27]
	v_mfma_f32_16x16x32_bf16 v[12:15], v[112:115], v[202:205], v[12:15]
	v_mfma_f32_16x16x32_bf16 v[8:11], v[124:127], v[202:205], v[8:11]
	s_setprio 0
	s_setprio 1
	v_mfma_f32_16x16x32_bf16 v[52:55], v[158:161], v[174:177], v[52:55]
	v_mfma_f32_16x16x32_bf16 v[48:51], v[166:169], v[174:177], v[48:51]
	v_mfma_f32_16x16x32_bf16 v[36:39], v[158:161], v[182:185], v[36:39]
	v_mfma_f32_16x16x32_bf16 v[32:35], v[166:169], v[182:185], v[32:35]
	v_mfma_f32_16x16x32_bf16 v[20:23], v[158:161], v[190:193], v[20:23]
	v_mfma_f32_16x16x32_bf16 v[16:19], v[166:169], v[190:193], v[16:19]
	v_mfma_f32_16x16x32_bf16 v[4:7], v[158:161], v[198:201], v[4:7]
	v_mfma_f32_16x16x32_bf16 v[0:3], v[166:169], v[198:201], v[0:3]
	v_mfma_f32_16x16x32_bf16 v[52:55], v[162:165], v[178:181], v[52:55]
	v_mfma_f32_16x16x32_bf16 v[48:51], v[170:173], v[178:181], v[48:51]
	v_mfma_f32_16x16x32_bf16 v[36:39], v[162:165], v[186:189], v[36:39]
	v_mfma_f32_16x16x32_bf16 v[32:35], v[170:173], v[186:189], v[32:35]
	v_mfma_f32_16x16x32_bf16 v[20:23], v[162:165], v[194:197], v[20:23]
	v_mfma_f32_16x16x32_bf16 v[16:19], v[170:173], v[194:197], v[16:19]
	v_mfma_f32_16x16x32_bf16 v[4:7], v[162:165], v[202:205], v[4:7]
	v_mfma_f32_16x16x32_bf16 v[0:3], v[170:173], v[202:205], v[0:3]
	s_setprio 0
	v_add_u32_e32 v124, s28, v156
	v_add_u32_e32 v170, s45, v156
	s_add_i32 s78, s78, 2
	s_add_u32 s76, s76, 0x10000
	s_addc_u32 s77, s77, 0
	s_mov_b64 s[0:1], s[46:47]
	s_cmp_gt_u32 s78, 29
	s_barrier
	s_cbranch_scc0 .LBB0_1173
	s_and_b64 vcc, exec, s[24:25]
	s_cbranch_vccz .LBB0_1176
	s_barrier

.LBB0_1248:
	ds_read_b128 v[72:75], v92
	ds_read_b128 v[76:79], v92 offset:1024
	ds_read_b128 v[84:87], v92 offset:2048
	ds_read_b128 v[92:95], v92 offset:3072
	ds_read_b128 v[144:147], v156
	ds_read_b128 v[148:151], v156 offset:1024
	ds_read_b128 v[152:155], v156 offset:2048
	ds_read_b128 v[156:159], v156 offset:3072
	s_add_u32 s44, s0, 0x10000
	s_addc_u32 s45, s1, 0
	s_cmpk_eq_i32 s76, 0x7c
	s_cselect_b32 s50, s5, s44
	s_cselect_b32 s51, s4, s45
	s_cselect_b32 s48, s35, s74
	s_cselect_b32 s49, s25, s75
	s_add_u32 s46, s50, 0x8000
	s_addc_u32 s47, s51, 0
	v_lshl_add_u64 v[204:205], s[0:1], 0, v[180:181]
	s_add_i32 m0, s56, 0xc000
	ds_read_b128 v[160:163], v207
	ds_read_b128 v[164:167], v207 offset:1024
	ds_read_b128 v[168:171], v207 offset:2048
	ds_read_b128 v[184:187], v207 offset:3072
	ds_read_b128 v[188:191], v207 offset:4096
	ds_read_b128 v[192:195], v207 offset:5120
	ds_read_b128 v[196:199], v207 offset:6144
	ds_read_b128 v[200:203], v207 offset:7168
	global_load_lds_dwordx4 v[204:205], off
	v_lshl_add_u64 v[204:205], s[0:1], 0, v[182:183]
	s_add_i32 m0, s56, 0xe000
	s_nop 0
	global_load_lds_dwordx4 v[204:205], off
	s_waitcnt vmcnt(8)
	s_and_b64 vcc, exec, s[22:23]
	s_cbranch_vccnz .Llead_skip_3_0
	s_waitcnt lgkmcnt(0)

.Llead_skip_3_3:
	s_barrier
	s_setprio 1
	s_waitcnt lgkmcnt(0)
	v_mfma_f32_16x16x32_bf16 v[60:63], v[72:75], v[160:163], v[60:63]
	v_mfma_f32_16x16x32_bf16 v[56:59], v[84:87], v[160:163], v[56:59]
	v_mfma_f32_16x16x32_bf16 v[44:47], v[72:75], v[168:171], v[44:47]
	v_mfma_f32_16x16x32_bf16 v[40:43], v[84:87], v[168:171], v[40:43]
	v_mfma_f32_16x16x32_bf16 v[28:31], v[72:75], v[188:191], v[28:31]
	v_mfma_f32_16x16x32_bf16 v[24:27], v[84:87], v[188:191], v[24:27]
	v_mfma_f32_16x16x32_bf16 v[12:15], v[72:75], v[196:199], v[12:15]
	v_mfma_f32_16x16x32_bf16 v[8:11], v[84:87], v[196:199], v[8:11]
	v_mfma_f32_16x16x32_bf16 v[60:63], v[76:79], v[164:167], v[60:63]
	v_mfma_f32_16x16x32_bf16 v[56:59], v[92:95], v[164:167], v[56:59]
	v_mfma_f32_16x16x32_bf16 v[44:47], v[76:79], v[184:187], v[44:47]
	v_mfma_f32_16x16x32_bf16 v[40:43], v[92:95], v[184:187], v[40:43]
	v_mfma_f32_16x16x32_bf16 v[28:31], v[76:79], v[192:195], v[28:31]
	v_mfma_f32_16x16x32_bf16 v[24:27], v[92:95], v[192:195], v[24:27]
	v_mfma_f32_16x16x32_bf16 v[12:15], v[76:79], v[200:203], v[12:15]
	v_mfma_f32_16x16x32_bf16 v[8:11], v[92:95], v[200:203], v[8:11]
	s_setprio 0
	s_setprio 1
	v_mfma_f32_16x16x32_bf16 v[52:55], v[144:147], v[160:163], v[52:55]
	v_mfma_f32_16x16x32_bf16 v[48:51], v[152:155], v[160:163], v[48:51]
	v_mfma_f32_16x16x32_bf16 v[36:39], v[144:147], v[168:171], v[36:39]
	v_mfma_f32_16x16x32_bf16 v[32:35], v[152:155], v[168:171], v[32:35]
	v_mfma_f32_16x16x32_bf16 v[20:23], v[144:147], v[188:191], v[20:23]
	v_mfma_f32_16x16x32_bf16 v[16:19], v[152:155], v[188:191], v[16:19]
	v_mfma_f32_16x16x32_bf16 v[4:7], v[144:147], v[196:199], v[4:7]
	v_mfma_f32_16x16x32_bf16 v[0:3], v[152:155], v[196:199], v[0:3]
	v_mfma_f32_16x16x32_bf16 v[52:55], v[148:151], v[164:167], v[52:55]
	v_mfma_f32_16x16x32_bf16 v[48:51], v[156:159], v[164:167], v[48:51]
	v_mfma_f32_16x16x32_bf16 v[36:39], v[148:151], v[184:187], v[36:39]
	v_mfma_f32_16x16x32_bf16 v[32:35], v[156:159], v[184:187], v[32:35]
	v_mfma_f32_16x16x32_bf16 v[20:23], v[148:151], v[192:195], v[20:23]
	v_mfma_f32_16x16x32_bf16 v[16:19], v[156:159], v[192:195], v[16:19]
	v_mfma_f32_16x16x32_bf16 v[4:7], v[148:151], v[200:203], v[4:7]
	v_mfma_f32_16x16x32_bf16 v[0:3], v[156:159], v[200:203], v[0:3]
	s_setprio 0
	v_add_u32_e32 v92, s30, v206
	v_add_u32_e32 v156, s52, v206
	s_add_i32 s76, s76, 2
	s_add_u32 s74, s74, 0x10000
	s_addc_u32 s75, s75, 0
	s_mov_b64 s[0:1], s[44:45]
	s_cmpk_gt_u32 s76, 0x7d
	s_barrier
	s_cbranch_scc0 .LBB0_1248
	s_and_b64 vcc, exec, s[22:23]
	s_cbranch_vccz .LBB0_1251
	s_barrier
